# pk_final + nontemporal hint on FINAL phase output stores and expert-output row loads (streamed once)
# speedup vs baseline: 1.0013x; 1.0013x over previous
.LBB0_2219:
	s_add_u32 s14, s50, s6
	s_addc_u32 s15, s51, s7
	global_load_dwordx4 v[2:5], v[44:45], off
	global_load_dwordx4 v[6:9], v[44:45], off offset:1024
	global_load_dwordx4 v[10:13], v[44:45], off offset:2048
	global_load_dwordx4 v[14:17], v[44:45], off offset:3072
	global_load_dwordx4 v[18:21], v[48:49], off
	global_load_dwordx4 v[22:25], v[50:51], off
	global_load_dwordx4 v[26:29], v[52:53], off
	global_load_dwordx4 v[30:33], v[54:55], off
	global_load_dwordx4 v[34:37], v[46:47], off
	global_load_dwordx4 v[74:77], v73, s[14:15]
	global_load_dwordx4 v[38:41], v1, s[14:15]
	v_add_co_u32_e32 v70, vcc, s3, v64
	v_lshl_add_u64 v[68:69], s[50:51], 0, v[66:67]
	s_nop 0
	v_addc_co_u32_e32 v71, vcc, -1, v65, vcc
	v_add_co_u32_e32 v68, vcc, 0x577d0000, v68
	v_mov_b32_e32 v195, 0
	s_nop 0
	v_addc_co_u32_e32 v69, vcc, 0, v69, vcc
	global_load_dwordx2 v[78:79], v[68:69], off nt
	global_load_dwordx2 v[80:81], v[68:69], off offset:512 nt
	global_load_dwordx2 v[82:83], v[68:69], off offset:1024 nt
	global_load_dwordx2 v[86:87], v[68:69], off offset:1536 nt
	global_load_dwordx2 v[92:93], v[68:69], off offset:2048 nt
	global_load_dwordx2 v[94:95], v[68:69], off offset:2560 nt
	global_load_dwordx2 v[96:97], v[68:69], off offset:3072 nt
	global_load_dwordx2 v[98:99], v[68:69], off offset:3584 nt
	v_mov_b32_e32 v236, 0
	s_add_i32 s0, s0, s4
	s_add_u32 s6, s6, s8
	s_addc_u32 s7, s7, s9
	v_lshl_add_u64 v[66:67], v[66:67], 0, s[12:13]
	s_cmpk_lt_i32 s0, 0x4000
	s_waitcnt vmcnt(9)
	v_ashrrev_i32_e32 v101, 31, v74
	v_mov_b32_e32 v100, v74
	v_ashrrev_i32_e32 v103, 31, v75
	v_mov_b32_e32 v102, v75
	v_ashrrev_i32_e32 v105, 31, v76
	v_mov_b32_e32 v104, v76
	v_ashrrev_i32_e32 v107, 31, v77
	v_mov_b32_e32 v106, v77
	v_lshlrev_b64 v[102:103], 12, v[102:103]
	v_lshlrev_b64 v[100:101], 12, v[100:101]
	v_lshlrev_b64 v[106:107], 12, v[106:107]
	v_lshlrev_b64 v[104:105], 12, v[104:105]
	v_lshl_add_u64 v[100:101], v[42:43], 0, v[100:101]
	v_lshl_add_u64 v[102:103], v[42:43], 0, v[102:103]
	v_lshl_add_u64 v[104:105], v[42:43], 0, v[104:105]
	v_lshl_add_u64 v[106:107], v[42:43], 0, v[106:107]
	global_load_dwordx2 v[114:115], v[100:101], off nt
	global_load_dwordx2 v[116:117], v[102:103], off nt
	global_load_dwordx2 v[118:119], v[104:105], off nt
	global_load_dwordx2 v[120:121], v[106:107], off nt
	global_load_dwordx2 v[122:123], v[100:101], off offset:512 nt
	global_load_dwordx2 v[124:125], v[102:103], off offset:512 nt
	global_load_dwordx2 v[126:127], v[104:105], off offset:512 nt
	global_load_dwordx2 v[128:129], v[106:107], off offset:512 nt
	global_load_dwordx2 v[130:131], v[100:101], off offset:1024 nt
	global_load_dwordx2 v[132:133], v[102:103], off offset:1024 nt
	global_load_dwordx2 v[134:135], v[104:105], off offset:1024 nt
	global_load_dwordx2 v[136:137], v[106:107], off offset:1024 nt
	global_load_dwordx2 v[138:139], v[100:101], off offset:1536 nt
	global_load_dwordx2 v[140:141], v[102:103], off offset:1536 nt
	global_load_dwordx2 v[142:143], v[104:105], off offset:1536 nt
	global_load_dwordx2 v[144:145], v[106:107], off offset:1536 nt
	global_load_dwordx2 v[146:147], v[100:101], off offset:2048 nt
	global_load_dwordx2 v[148:149], v[102:103], off offset:2048 nt
	global_load_dwordx2 v[150:151], v[104:105], off offset:2048 nt
	global_load_dwordx2 v[152:153], v[100:101], off offset:2560 nt
	global_load_dwordx2 v[154:155], v[100:101], off offset:3072 nt
	s_nop 0
	global_load_dwordx2 v[100:101], v[100:101], off offset:3584 nt
	s_nop 0
	global_load_dwordx2 v[156:157], v[106:107], off offset:2048 nt
	global_load_dwordx2 v[158:159], v[102:103], off offset:2560 nt
	global_load_dwordx2 v[160:161], v[102:103], off offset:3072 nt
	s_nop 0
	global_load_dwordx2 v[102:103], v[102:103], off offset:3584 nt
	s_nop 0
	global_load_dwordx2 v[162:163], v[104:105], off offset:2560 nt
	global_load_dwordx2 v[164:165], v[104:105], off offset:3072 nt
	s_nop 0
	global_load_dwordx2 v[104:105], v[104:105], off offset:3584 nt
	s_nop 0
	global_load_dwordx2 v[166:167], v[106:107], off offset:2560 nt
	global_load_dwordx2 v[168:169], v[106:107], off offset:3072 nt
	s_nop 0
	global_load_dwordx2 v[106:107], v[106:107], off offset:3584 nt
	s_waitcnt vmcnt(40)
	v_mov_b32_e32 v72, v41
	s_waitcnt vmcnt(39)
	v_lshlrev_b32_e32 v68, 16, v78
	v_and_b32_e32 v69, 0xffff0000, v78
	v_lshlrev_b32_e32 v76, 16, v79
	v_and_b32_e32 v77, 0xffff0000, v79
	s_waitcnt vmcnt(38)
	v_lshlrev_b32_e32 v74, 16, v80
	v_and_b32_e32 v75, 0xffff0000, v80
	v_lshlrev_b32_e32 v80, 16, v81
	v_and_b32_e32 v81, 0xffff0000, v81
	s_waitcnt vmcnt(37)
	v_lshlrev_b32_e32 v78, 16, v82
	v_and_b32_e32 v79, 0xffff0000, v82
	v_lshlrev_b32_e32 v84, 16, v83
	v_and_b32_e32 v85, 0xffff0000, v83
	s_waitcnt vmcnt(32)
	v_lshlrev_b32_e32 v112, 16, v98
	v_and_b32_e32 v113, 0xffff0000, v98
	v_lshlrev_b32_e32 v98, 16, v99
	v_and_b32_e32 v99, 0xffff0000, v99
	v_lshlrev_b32_e32 v82, 16, v86
	v_and_b32_e32 v83, 0xffff0000, v86
	v_lshlrev_b32_e32 v88, 16, v87
	v_and_b32_e32 v89, 0xffff0000, v87
	v_lshlrev_b32_e32 v86, 16, v92
	v_and_b32_e32 v87, 0xffff0000, v92
	v_lshlrev_b32_e32 v92, 16, v93
	v_and_b32_e32 v93, 0xffff0000, v93
	v_lshlrev_b32_e32 v108, 16, v94
	v_and_b32_e32 v109, 0xffff0000, v94
	v_lshlrev_b32_e32 v94, 16, v95
	v_and_b32_e32 v95, 0xffff0000, v95
	v_lshlrev_b32_e32 v110, 16, v96
	v_and_b32_e32 v111, 0xffff0000, v96
	v_lshlrev_b32_e32 v96, 16, v97
	v_and_b32_e32 v97, 0xffff0000, v97
	s_waitcnt vmcnt(31)
	v_lshlrev_b32_e32 v170, 16, v114
	v_and_b32_e32 v171, 0xffff0000, v114
	v_lshlrev_b32_e32 v114, 16, v115
	v_and_b32_e32 v115, 0xffff0000, v115
	s_waitcnt vmcnt(27)
	v_lshlrev_b32_e32 v178, 16, v122
	v_and_b32_e32 v179, 0xffff0000, v122
	v_lshlrev_b32_e32 v122, 16, v123
	v_and_b32_e32 v123, 0xffff0000, v123
	v_lshlrev_b32_e32 v172, 16, v116
	v_and_b32_e32 v173, 0xffff0000, v116
	v_lshlrev_b32_e32 v116, 16, v117
	v_and_b32_e32 v117, 0xffff0000, v117
	s_waitcnt vmcnt(26)
	v_lshlrev_b32_e32 v180, 16, v124
	v_and_b32_e32 v181, 0xffff0000, v124
	v_lshlrev_b32_e32 v124, 16, v125
	v_and_b32_e32 v125, 0xffff0000, v125
	s_waitcnt vmcnt(23)
	v_lshlrev_b32_e32 v186, 16, v130
	v_and_b32_e32 v187, 0xffff0000, v130
	v_lshlrev_b32_e32 v130, 16, v131
	v_and_b32_e32 v131, 0xffff0000, v131
	s_waitcnt vmcnt(19)
	v_lshlrev_b32_e32 v196, 16, v138
	v_and_b32_e32 v197, 0xffff0000, v138
	v_lshlrev_b32_e32 v138, 16, v139
	v_and_b32_e32 v139, 0xffff0000, v139
	s_waitcnt vmcnt(15)
	v_lshlrev_b32_e32 v204, 16, v146
	v_and_b32_e32 v205, 0xffff0000, v146
	v_lshlrev_b32_e32 v146, 16, v147
	v_and_b32_e32 v147, 0xffff0000, v147
	s_waitcnt vmcnt(12)
	v_lshlrev_b32_e32 v212, 16, v152
	v_and_b32_e32 v213, 0xffff0000, v152
	v_lshlrev_b32_e32 v152, 16, v153
	v_and_b32_e32 v153, 0xffff0000, v153
	s_waitcnt vmcnt(11)
	v_lshlrev_b32_e32 v220, 16, v154
	v_and_b32_e32 v221, 0xffff0000, v154
	v_lshlrev_b32_e32 v154, 16, v155
	v_and_b32_e32 v155, 0xffff0000, v155
	s_waitcnt vmcnt(10)
	v_lshlrev_b32_e32 v228, 16, v100
	v_and_b32_e32 v229, 0xffff0000, v100
	v_lshlrev_b32_e32 v100, 16, v101
	v_and_b32_e32 v101, 0xffff0000, v101
	v_pk_fma_f32 v[170:171], v[38:39], v[170:171], 0 op_sel_hi:[0,1,0]
	v_pk_fma_f32 v[114:115], v[38:39], v[114:115], 0 op_sel_hi:[0,1,0]
	v_pk_fma_f32 v[178:179], v[38:39], v[178:179], 0 op_sel_hi:[0,1,0]
	v_pk_fma_f32 v[122:123], v[38:39], v[122:123], 0 op_sel_hi:[0,1,0]
	v_lshlrev_b32_e32 v174, 16, v118
	v_and_b32_e32 v175, 0xffff0000, v118
	v_lshlrev_b32_e32 v118, 16, v119
	v_and_b32_e32 v119, 0xffff0000, v119
	v_lshlrev_b32_e32 v182, 16, v126
	v_and_b32_e32 v183, 0xffff0000, v126
	v_lshlrev_b32_e32 v126, 16, v127
	v_and_b32_e32 v127, 0xffff0000, v127
	v_lshlrev_b32_e32 v188, 16, v132
	v_and_b32_e32 v189, 0xffff0000, v132
	v_lshlrev_b32_e32 v132, 16, v133
	v_and_b32_e32 v133, 0xffff0000, v133
	v_lshlrev_b32_e32 v198, 16, v140
	v_and_b32_e32 v199, 0xffff0000, v140
	v_lshlrev_b32_e32 v140, 16, v141
	v_and_b32_e32 v141, 0xffff0000, v141
	v_lshlrev_b32_e32 v206, 16, v148
	v_and_b32_e32 v207, 0xffff0000, v148
	v_lshlrev_b32_e32 v148, 16, v149
	v_and_b32_e32 v149, 0xffff0000, v149
	s_waitcnt vmcnt(8)
	v_lshlrev_b32_e32 v214, 16, v158
	v_and_b32_e32 v215, 0xffff0000, v158
	v_lshlrev_b32_e32 v158, 16, v159
	v_and_b32_e32 v159, 0xffff0000, v159
	s_waitcnt vmcnt(7)
	v_lshlrev_b32_e32 v222, 16, v160
	v_and_b32_e32 v223, 0xffff0000, v160
	v_lshlrev_b32_e32 v160, 16, v161
	v_and_b32_e32 v161, 0xffff0000, v161
	s_waitcnt vmcnt(6)
	v_lshlrev_b32_e32 v230, 16, v102
	v_and_b32_e32 v231, 0xffff0000, v102
	v_lshlrev_b32_e32 v102, 16, v103
	v_and_b32_e32 v103, 0xffff0000, v103
	v_pk_fma_f32 v[186:187], v[38:39], v[186:187], 0 op_sel_hi:[0,1,0]
	v_pk_fma_f32 v[130:131], v[38:39], v[130:131], 0 op_sel_hi:[0,1,0]
	v_pk_fma_f32 v[196:197], v[38:39], v[196:197], 0 op_sel_hi:[0,1,0]
	v_pk_fma_f32 v[138:139], v[38:39], v[138:139], 0 op_sel_hi:[0,1,0]
	v_pk_fma_f32 v[204:205], v[38:39], v[204:205], 0 op_sel_hi:[0,1,0]
	v_pk_fma_f32 v[146:147], v[38:39], v[146:147], 0 op_sel_hi:[0,1,0]
	v_pk_fma_f32 v[212:213], v[38:39], v[212:213], 0 op_sel_hi:[0,1,0]
	v_pk_fma_f32 v[152:153], v[38:39], v[152:153], 0 op_sel_hi:[0,1,0]
	v_pk_fma_f32 v[220:221], v[38:39], v[220:221], 0 op_sel_hi:[0,1,0]
	v_pk_fma_f32 v[154:155], v[38:39], v[154:155], 0 op_sel_hi:[0,1,0]
	v_pk_fma_f32 v[228:229], v[38:39], v[228:229], 0 op_sel_hi:[0,1,0]
	v_pk_fma_f32 v[100:101], v[38:39], v[100:101], 0 op_sel_hi:[0,1,0]
	v_pk_fma_f32 v[170:171], v[38:39], v[172:173], v[170:171] op_sel:[1,0,0]
	v_pk_fma_f32 v[114:115], v[38:39], v[116:117], v[114:115] op_sel:[1,0,0]
	v_pk_fma_f32 v[116:117], v[38:39], v[180:181], v[178:179] op_sel:[1,0,0]
	v_pk_fma_f32 v[122:123], v[38:39], v[124:125], v[122:123] op_sel:[1,0,0]
	v_lshlrev_b32_e32 v176, 16, v120
	v_and_b32_e32 v177, 0xffff0000, v120
	v_lshlrev_b32_e32 v120, 16, v121
	v_and_b32_e32 v121, 0xffff0000, v121
	v_lshlrev_b32_e32 v184, 16, v128
	v_and_b32_e32 v185, 0xffff0000, v128
	v_lshlrev_b32_e32 v128, 16, v129
	v_and_b32_e32 v129, 0xffff0000, v129
	v_lshlrev_b32_e32 v190, 16, v134
	v_and_b32_e32 v191, 0xffff0000, v134
	v_lshlrev_b32_e32 v134, 16, v135
	v_and_b32_e32 v135, 0xffff0000, v135
	v_lshlrev_b32_e32 v200, 16, v142
	v_and_b32_e32 v201, 0xffff0000, v142
	v_lshlrev_b32_e32 v142, 16, v143
	v_and_b32_e32 v143, 0xffff0000, v143
	v_lshlrev_b32_e32 v208, 16, v150
	v_and_b32_e32 v209, 0xffff0000, v150
	v_lshlrev_b32_e32 v150, 16, v151
	v_and_b32_e32 v151, 0xffff0000, v151
	s_waitcnt vmcnt(5)
	v_lshlrev_b32_e32 v216, 16, v162
	v_and_b32_e32 v217, 0xffff0000, v162
	v_lshlrev_b32_e32 v162, 16, v163
	v_and_b32_e32 v163, 0xffff0000, v163
	s_waitcnt vmcnt(4)
	v_lshlrev_b32_e32 v224, 16, v164
	v_and_b32_e32 v225, 0xffff0000, v164
	v_lshlrev_b32_e32 v164, 16, v165
	v_and_b32_e32 v165, 0xffff0000, v165
	s_waitcnt vmcnt(3)
	v_lshlrev_b32_e32 v232, 16, v104
	v_and_b32_e32 v233, 0xffff0000, v104
	v_lshlrev_b32_e32 v104, 16, v105
	v_and_b32_e32 v105, 0xffff0000, v105
	v_pk_fma_f32 v[124:125], v[38:39], v[188:189], v[186:187] op_sel:[1,0,0]
	v_pk_fma_f32 v[130:131], v[38:39], v[132:133], v[130:131] op_sel:[1,0,0]
	v_pk_fma_f32 v[132:133], v[38:39], v[198:199], v[196:197] op_sel:[1,0,0]
	v_pk_fma_f32 v[138:139], v[38:39], v[140:141], v[138:139] op_sel:[1,0,0]
	v_pk_fma_f32 v[140:141], v[38:39], v[206:207], v[204:205] op_sel:[1,0,0]
	v_pk_fma_f32 v[146:147], v[38:39], v[148:149], v[146:147] op_sel:[1,0,0]
	v_pk_fma_f32 v[148:149], v[38:39], v[214:215], v[212:213] op_sel:[1,0,0]
	v_pk_fma_f32 v[152:153], v[38:39], v[158:159], v[152:153] op_sel:[1,0,0]
	v_pk_fma_f32 v[158:159], v[38:39], v[222:223], v[220:221] op_sel:[1,0,0]
	v_pk_fma_f32 v[154:155], v[38:39], v[160:161], v[154:155] op_sel:[1,0,0]
	v_pk_fma_f32 v[160:161], v[38:39], v[230:231], v[228:229] op_sel:[1,0,0]
	v_pk_fma_f32 v[38:39], v[38:39], v[102:103], v[100:101] op_sel:[1,0,0]
	v_pk_fma_f32 v[100:101], v[40:41], v[174:175], v[170:171] op_sel_hi:[0,1,1]
	v_pk_fma_f32 v[102:103], v[40:41], v[118:119], v[114:115] op_sel_hi:[0,1,1]
	v_pk_fma_f32 v[114:115], v[40:41], v[182:183], v[116:117] op_sel_hi:[0,1,1]
	v_pk_fma_f32 v[116:117], v[40:41], v[126:127], v[122:123] op_sel_hi:[0,1,1]
	v_lshlrev_b32_e32 v192, 16, v136
	v_and_b32_e32 v193, 0xffff0000, v136
	v_lshlrev_b32_e32 v136, 16, v137
	v_and_b32_e32 v137, 0xffff0000, v137
	v_pk_fma_f32 v[118:119], v[40:41], v[190:191], v[124:125] op_sel_hi:[0,1,1]
	v_pk_fma_f32 v[122:123], v[40:41], v[134:135], v[130:131] op_sel_hi:[0,1,1]
	v_pk_fma_f32 v[124:125], v[40:41], v[200:201], v[132:133] op_sel_hi:[0,1,1]
	v_pk_fma_f32 v[126:127], v[40:41], v[142:143], v[138:139] op_sel_hi:[0,1,1]
	v_pk_fma_f32 v[130:131], v[40:41], v[208:209], v[140:141] op_sel_hi:[0,1,1]
	v_pk_fma_f32 v[132:133], v[40:41], v[150:151], v[146:147] op_sel_hi:[0,1,1]
	v_pk_fma_f32 v[134:135], v[40:41], v[216:217], v[148:149] op_sel_hi:[0,1,1]
	v_pk_fma_f32 v[138:139], v[40:41], v[162:163], v[152:153] op_sel_hi:[0,1,1]
	v_pk_fma_f32 v[140:141], v[40:41], v[224:225], v[158:159] op_sel_hi:[0,1,1]
	v_pk_fma_f32 v[142:143], v[40:41], v[164:165], v[154:155] op_sel_hi:[0,1,1]
	v_pk_fma_f32 v[146:147], v[40:41], v[232:233], v[160:161] op_sel_hi:[0,1,1]
	v_pk_fma_f32 v[38:39], v[40:41], v[104:105], v[38:39] op_sel_hi:[0,1,1]
	v_pk_fma_f32 v[40:41], v[72:73], v[176:177], v[100:101] op_sel_hi:[0,1,1]
	v_pk_fma_f32 v[100:101], v[72:73], v[120:121], v[102:103] op_sel_hi:[0,1,1]
	v_pk_fma_f32 v[102:103], v[72:73], v[184:185], v[114:115] op_sel_hi:[0,1,1]
	v_pk_fma_f32 v[104:105], v[72:73], v[128:129], v[116:117] op_sel_hi:[0,1,1]
	s_waitcnt vmcnt(0)
	v_lshlrev_b32_e32 v234, 16, v106
	v_and_b32_e32 v235, 0xffff0000, v106
	v_lshlrev_b32_e32 v106, 16, v107
	v_and_b32_e32 v107, 0xffff0000, v107
	v_pk_fma_f32 v[114:115], v[72:73], v[192:193], v[118:119] op_sel_hi:[0,1,1]
	v_pk_fma_f32 v[116:117], v[72:73], v[136:137], v[122:123] op_sel_hi:[0,1,1]
	v_pk_fma_f32 v[4:5], v[100:101], v[4:5], v[76:77]
	v_pk_fma_f32 v[2:3], v[40:41], v[2:3], v[68:69]
	v_pk_fma_f32 v[8:9], v[104:105], v[8:9], v[80:81]
	v_pk_fma_f32 v[6:7], v[102:103], v[6:7], v[74:75]
	v_lshlrev_b32_e32 v202, 16, v144
	v_and_b32_e32 v203, 0xffff0000, v144
	v_lshlrev_b32_e32 v144, 16, v145
	v_and_b32_e32 v145, 0xffff0000, v145
	v_lshlrev_b32_e32 v210, 16, v156
	v_and_b32_e32 v211, 0xffff0000, v156
	v_lshlrev_b32_e32 v156, 16, v157
	v_and_b32_e32 v157, 0xffff0000, v157
	v_pk_fma_f32 v[38:39], v[72:73], v[106:107], v[38:39] op_sel_hi:[0,1,1]
	v_pk_fma_f32 v[10:11], v[114:115], v[10:11], v[78:79]
	v_pk_fma_f32 v[12:13], v[116:117], v[12:13], v[84:85]
	v_mov_b32_e32 v40, v3
	v_mov_b32_e32 v41, v7
	v_mov_b32_e32 v74, v5
	v_mov_b32_e32 v75, v9
	v_pk_fma_f32 v[118:119], v[72:73], v[202:203], v[124:125] op_sel_hi:[0,1,1]
	v_pk_fma_f32 v[120:121], v[72:73], v[144:145], v[126:127] op_sel_hi:[0,1,1]
	v_pk_fma_f32 v[124:125], v[72:73], v[156:157], v[132:133] op_sel_hi:[0,1,1]
	v_pk_fma_f32 v[32:33], v[38:39], v[32:33], v[98:99]
	v_mov_b32_e32 v38, v2
	v_mov_b32_e32 v39, v6
	v_mov_b32_e32 v68, v4
	v_mov_b32_e32 v69, v8
	v_pk_mul_f32 v[76:77], v[12:13], v[12:13]
	v_pk_mul_f32 v[78:79], v[10:11], v[10:11]
	v_pk_mul_f32 v[40:41], v[40:41], v[40:41]
	v_pk_mul_f32 v[74:75], v[74:75], v[74:75]
	v_lshlrev_b32_e32 v218, 16, v166
	v_and_b32_e32 v219, 0xffff0000, v166
	v_lshlrev_b32_e32 v166, 16, v167
	v_and_b32_e32 v167, 0xffff0000, v167
	v_lshlrev_b32_e32 v226, 16, v168
	v_and_b32_e32 v227, 0xffff0000, v168
	v_lshlrev_b32_e32 v168, 16, v169
	v_and_b32_e32 v169, 0xffff0000, v169
	v_pk_fma_f32 v[122:123], v[72:73], v[210:211], v[130:131] op_sel_hi:[0,1,1]
	v_pk_fma_f32 v[16:17], v[120:121], v[16:17], v[88:89]
	v_pk_fma_f32 v[14:15], v[118:119], v[14:15], v[82:83]
	v_pk_fma_f32 v[20:21], v[124:125], v[20:21], v[92:93]
	v_pk_mov_b32 v[92:93], v[78:79], v[76:77] op_sel:[1,0]
	v_mov_b32_e32 v79, v77
	v_pk_fma_f32 v[38:39], v[38:39], v[38:39], v[40:41]
	v_pk_fma_f32 v[40:41], v[68:69], v[68:69], v[74:75]
	v_pk_fma_f32 v[126:127], v[72:73], v[218:219], v[134:135] op_sel_hi:[0,1,1]
	v_pk_fma_f32 v[128:129], v[72:73], v[166:167], v[138:139] op_sel_hi:[0,1,1]
	v_pk_fma_f32 v[130:131], v[72:73], v[226:227], v[140:141] op_sel_hi:[0,1,1]
	v_pk_fma_f32 v[132:133], v[72:73], v[168:169], v[142:143] op_sel_hi:[0,1,1]
	v_pk_fma_f32 v[134:135], v[72:73], v[234:235], v[146:147] op_sel_hi:[0,1,1]
	v_pk_fma_f32 v[18:19], v[122:123], v[18:19], v[86:87]
	v_mul_f32_e32 v72, v15, v15
	v_mul_f32_e32 v80, v17, v17
	v_pk_add_f32 v[68:69], v[92:93], v[78:79]
	v_pk_add_f32 v[38:39], v[38:39], v[40:41]
	v_pk_fma_f32 v[22:23], v[126:127], v[22:23], v[108:109]
	v_pk_fma_f32 v[24:25], v[128:129], v[24:25], v[94:95]
	v_pk_fma_f32 v[28:29], v[132:133], v[28:29], v[96:97]
	v_mul_f32_e32 v89, v18, v18
	v_mul_f32_e32 v96, v19, v19
	v_mul_f32_e32 v97, v20, v20
	v_mul_f32_e32 v98, v21, v21
	v_pk_fma_f32 v[76:77], v[14:15], v[14:15], v[72:73] op_sel_hi:[1,1,0]
	v_pk_fma_f32 v[80:81], v[16:17], v[16:17], v[80:81] op_sel_hi:[1,1,0]
	v_pk_add_f32 v[40:41], v[68:69], v[68:69] op_sel:[0,1] op_sel_hi:[1,0]
	v_pk_add_f32 v[38:39], v[38:39], v[38:39] op_sel:[0,1] op_sel_hi:[1,0]
	v_pk_mul_f32 v[82:83], v[24:25], v[24:25]
	v_pk_mul_f32 v[84:85], v[22:23], v[22:23]
	v_mov_b32_e32 v77, v97
	v_mov_b32_e32 v81, v98
	v_mov_b32_e32 v41, v96
	v_mov_b32_e32 v39, v89
	v_pk_fma_f32 v[26:27], v[130:131], v[26:27], v[110:111]
	v_pk_mov_b32 v[94:95], v[84:85], v[82:83] op_sel:[1,0]
	v_mov_b32_e32 v85, v83
	v_pk_add_f32 v[68:69], v[76:77], v[80:81]
	v_pk_add_f32 v[38:39], v[38:39], v[40:41]
	v_pk_fma_f32 v[30:31], v[134:135], v[30:31], v[112:113]
	v_mul_f32_e32 v86, v27, v27
	v_mul_f32_e32 v88, v29, v29
	v_pk_add_f32 v[74:75], v[94:95], v[84:85]
	v_pk_add_f32 v[38:39], v[38:39], v[68:69]
	v_mul_f32_e32 v99, v30, v30
	v_mul_f32_e32 v100, v31, v31
	v_mul_f32_e32 v101, v32, v32
	v_mul_f32_e32 v102, v33, v33
	v_pk_fma_f32 v[82:83], v[26:27], v[26:27], v[86:87] op_sel_hi:[1,1,0]
	v_pk_fma_f32 v[86:87], v[28:29], v[28:29], v[88:89] op_sel_hi:[1,1,0]
	v_pk_add_f32 v[74:75], v[74:75], v[74:75] op_sel:[0,1] op_sel_hi:[1,0]
	v_pk_add_f32 v[38:39], v[38:39], v[38:39] op_sel:[0,1] op_sel_hi:[1,0]
	v_mov_b32_e32 v83, v101
	v_mov_b32_e32 v87, v102
	v_mov_b32_e32 v75, v100
	v_mov_b32_e32 v39, v99
	v_pk_add_f32 v[76:77], v[82:83], v[86:87]
	global_load_dwordx4 v[100:103], v[46:47], off offset:1024
	global_load_dwordx4 v[104:107], v[46:47], off offset:2048
	global_load_dwordx4 v[108:111], v[46:47], off offset:3072
	global_load_dwordx4 v[112:115], v[56:57], off
	global_load_dwordx4 v[116:119], v[58:59], off
	global_load_dwordx4 v[120:123], v[60:61], off
	global_load_dwordx4 v[124:127], v[62:63], off
	v_pk_add_f32 v[38:39], v[38:39], v[74:75]
	s_nop 0
	v_pk_add_f32 v[38:39], v[38:39], v[76:77]
	s_nop 0
	v_add_f32_e32 v38, v38, v39
	s_nop 1
	v_add_f32_dpp v38, v38, v38 row_shr:1 row_mask:0xf bank_mask:0xf bound_ctrl:1
	s_nop 1
	v_add_f32_dpp v38, v38, v38 row_shr:2 row_mask:0xf bank_mask:0xf bound_ctrl:1
	s_nop 1
	v_add_f32_dpp v38, v38, v38 row_shr:4 row_mask:0xf bank_mask:0xf bound_ctrl:1
	s_nop 1
	v_add_f32_dpp v38, v38, v38 row_shr:8 row_mask:0xf bank_mask:0xf bound_ctrl:1
	s_nop 1
	v_mov_b32_dpp v195, v38 row_bcast:15 row_mask:0xa bank_mask:0xf
	v_add_f32_e32 v38, v38, v195
	s_nop 1
	v_mov_b32_dpp v236, v38 row_bcast:31 row_mask:0xc bank_mask:0xf
	v_add_f32_e32 v38, v38, v236
	s_nop 0
	v_readlane_b32 s5, v38, 63
	s_nop 1
	v_fma_f32 v38, s5, v91, v90
	v_mul_f32_e32 v39, 0x4b800000, v38
	v_cmp_gt_f32_e32 vcc, s1, v38
	s_nop 1
	v_cndmask_b32_e32 v38, v38, v39, vcc
	v_rsq_f32_e32 v38, v38
	s_nop 0
	v_mul_f32_e32 v39, 0x45800000, v38
	v_cndmask_b32_e32 v38, v38, v39, vcc
	v_pk_mul_f32 v[2:3], v[38:39], v[2:3] op_sel_hi:[0,1]
	v_pk_mul_f32 v[4:5], v[38:39], v[4:5] op_sel_hi:[0,1]
	v_pk_mul_f32 v[4:5], v[36:37], v[4:5]
	v_pk_mul_f32 v[2:3], v[34:35], v[2:3]
	global_store_dwordx4 v[70:71], v[2:5], off offset:-3072 nt
	v_pk_mul_f32 v[8:9], v[38:39], v[8:9] op_sel_hi:[0,1]
	v_pk_mul_f32 v[6:7], v[38:39], v[6:7] op_sel_hi:[0,1]
	s_waitcnt vmcnt(7)
	v_pk_mul_f32 v[2:3], v[100:101], v[6:7]
	v_pk_mul_f32 v[4:5], v[102:103], v[8:9]
	global_store_dwordx4 v[70:71], v[2:5], off offset:-2048 nt
	v_pk_mul_f32 v[6:7], v[38:39], v[12:13] op_sel_hi:[0,1]
	v_pk_mul_f32 v[8:9], v[38:39], v[10:11] op_sel_hi:[0,1]
	s_waitcnt vmcnt(7)
	v_pk_mul_f32 v[2:3], v[104:105], v[8:9]
	v_pk_mul_f32 v[4:5], v[106:107], v[6:7]
	global_store_dwordx4 v[70:71], v[2:5], off offset:-1024 nt
	v_pk_mul_f32 v[6:7], v[38:39], v[16:17] op_sel_hi:[0,1]
	v_pk_mul_f32 v[8:9], v[38:39], v[14:15] op_sel_hi:[0,1]
	s_waitcnt vmcnt(7)
	v_pk_mul_f32 v[2:3], v[108:109], v[8:9]
	v_pk_mul_f32 v[4:5], v[110:111], v[6:7]
	global_store_dwordx4 v[64:65], v[2:5], off offset:-4096 nt
	v_pk_mul_f32 v[6:7], v[38:39], v[20:21] op_sel_hi:[0,1]
	v_pk_mul_f32 v[8:9], v[38:39], v[18:19] op_sel_hi:[0,1]
	s_waitcnt vmcnt(7)
	v_pk_mul_f32 v[2:3], v[112:113], v[8:9]
	v_pk_mul_f32 v[4:5], v[114:115], v[6:7]
	global_store_dwordx4 v[64:65], v[2:5], off offset:-3072 nt
	v_pk_mul_f32 v[6:7], v[38:39], v[24:25] op_sel_hi:[0,1]
	v_pk_mul_f32 v[8:9], v[38:39], v[22:23] op_sel_hi:[0,1]
	s_waitcnt vmcnt(7)
	v_pk_mul_f32 v[2:3], v[116:117], v[8:9]
	v_pk_mul_f32 v[4:5], v[118:119], v[6:7]
	global_store_dwordx4 v[64:65], v[2:5], off offset:-2048 nt
	v_pk_mul_f32 v[6:7], v[38:39], v[28:29] op_sel_hi:[0,1]
	v_pk_mul_f32 v[8:9], v[38:39], v[26:27] op_sel_hi:[0,1]
	s_waitcnt vmcnt(7)
	v_pk_mul_f32 v[2:3], v[120:121], v[8:9]
	v_pk_mul_f32 v[4:5], v[122:123], v[6:7]
	global_store_dwordx4 v[64:65], v[2:5], off offset:-1024 nt
	v_pk_mul_f32 v[6:7], v[38:39], v[32:33] op_sel_hi:[0,1]
	v_pk_mul_f32 v[8:9], v[38:39], v[30:31] op_sel_hi:[0,1]
	s_waitcnt vmcnt(7)
	v_pk_mul_f32 v[2:3], v[124:125], v[8:9]
	v_pk_mul_f32 v[4:5], v[126:127], v[6:7]
	global_store_dwordx4 v[64:65], v[2:5], off nt
	v_lshl_add_u64 v[64:65], v[64:65], 0, s[10:11]
	s_cbranch_scc1 .LBB0_2219
